# layer-0 rowpass: next iteration's two input rows prefetched speculatively (predicted address = current + 2 rows, verified at the next iteration, fallback reload on mismatch)
# baseline (speedup 1.0000x reference)
.LBB0_146:
	s_and_b64 vcc, exec, s[38:39]
	s_cbranch_vccz .LBB0_153
	v_readlane_b32 s36, v252, 16
	s_mulk_i32 s4, 0x110
	s_mul_i32 s2, s2, 34
	s_ashr_i32 s7, s6, 31
	s_add_i32 s12, s6, 32
	v_readlane_b32 s37, v252, 17
	s_add_i32 s2, s4, s2
	s_lshl_b64 s[14:15], s[6:7], 10
	s_lshl_b64 s[6:7], s[6:7], 11
	v_mov_b32_e32 v54, 0
	v_lshl_add_u64 v[48:49], v[60:61], 2, s[36:37]
	s_add_i32 s2, s2, -2
	v_lshl_add_u64 v[50:51], s[14:15], 0, v[60:61]
	v_lshl_add_u64 v[52:53], v[60:61], 1, s[6:7]
	s_mov_b32 s4, -1
	v_mov_b32_e32 v55, v54
	v_mov_b32_e32 v56, v54
	v_mov_b32_e32 v57, v54
	v_mov_b32_e32 v62, v54
	v_mov_b32_e32 v63, v54
	v_mov_b32_e32 v58, v54
	v_mov_b32_e32 v59, v54
	v_mov_b32_e32 v66, v54
	v_mov_b32_e32 v67, v54
	v_mov_b32_e32 v64, v54
	v_mov_b32_e32 v65, v54
	v_mov_b32_e32 v70, v54
	v_mov_b32_e32 v71, v54
	v_mov_b32_e32 v68, v54
	v_mov_b32_e32 v69, v54
	v_mov_b32_e32 v0, v54
	v_mov_b32_e32 v1, v54
	v_mov_b32_e32 v2, v54
	v_mov_b32_e32 v3, v54
	v_mov_b32_e32 v4, v54
	v_mov_b32_e32 v5, v54
	v_mov_b32_e32 v6, v54
	v_mov_b32_e32 v7, v54
	v_mov_b32_e32 v28, v54
	v_mov_b32_e32 v29, v54
	v_mov_b32_e32 v30, v54
	v_mov_b32_e32 v31, v54
	v_mov_b32_e32 v24, v54
	v_mov_b32_e32 v25, v54
	v_mov_b32_e32 v26, v54
	v_mov_b32_e32 v27, v54
	v_readlane_b32 s38, v252, 18
	v_readlane_b32 s39, v252, 19
	v_mov_b32_e32 v168, 0
	v_mov_b32_e32 v169, 0
	v_mov_b32_e32 v170, 0
	v_mov_b32_e32 v171, 0
	s_branch .LBB0_149

.LBB0_149:
	s_mov_b32 s25, s2
	s_add_i32 s2, s2, 2
	s_mul_hi_i32 s6, s2, 0x78787879
	s_lshr_b32 s7, s6, 31
	s_ashr_i32 s6, s6, 11
	s_add_i32 s6, s6, s7
	s_mul_i32 s7, s6, 0xffffef00
	s_add_i32 s28, s25, s7
	s_add_i32 s29, s28, 2
	s_cmpk_lt_i32 s29, 0x100
	s_cselect_b64 s[14:15], -1, 0
	s_and_b64 s[26:27], s[14:15], exec
	s_cselect_b32 s13, 16, s6
	s_ashr_i32 s7, s6, 31
	s_addk_i32 s28, 0xff02
	s_ashr_i32 s26, s29, 31
	s_and_b64 s[14:15], s[14:15], exec
	v_readlane_b32 s36, v252, 12
	v_readlane_b32 s40, v252, 14
	s_cselect_b32 s14, s29, s28
	v_readlane_b32 s37, v252, 13
	v_readlane_b32 s41, v252, 15
	s_cselect_b32 s28, 20, 24
	s_cselect_b32 s15, s26, 0
	s_cselect_b32 s26, s41, s37
	s_cselect_b32 s27, s40, s36
	s_lshl_b64 s[6:7], s[6:7], s28
	s_add_u32 s27, s27, s6
	s_addc_u32 s26, s26, s7
	s_lshl_b64 s[6:7], s[14:15], 12
	s_add_u32 s6, s27, s6
	s_addc_u32 s7, s26, s7
	v_lshlrev_b64 v[8:9], 2, v[60:61]
	v_lshl_add_u64 v[10:11], s[6:7], 0, v[8:9]
	s_add_i32 s6, s25, 3
	s_mul_hi_i32 s6, s6, 0x78787879
	s_lshr_b32 s7, s6, 31
	s_ashr_i32 s6, s6, 11
	s_add_i32 s6, s6, s7
	s_mul_i32 s7, s6, 0xffffef00
	s_add_i32 s14, s25, s7
	s_add_i32 s25, s14, 3
	s_cmpk_lt_i32 s25, 0x100
	s_cselect_b64 s[38:39], -1, 0
	s_ashr_i32 s7, s6, 31
	s_ashr_i32 s26, s25, 31
	s_add_i32 s27, s14, 0xffffff03
	s_and_b64 s[14:15], s[38:39], exec
	s_cselect_b32 s15, s26, 0
	s_cselect_b32 s26, 20, 24
	s_cselect_b32 s14, s25, s27
	s_cselect_b32 s25, s41, s37
	s_cselect_b32 s28, s40, s36
	s_lshl_b64 s[26:27], s[6:7], s26
	s_add_u32 s7, s28, s26
	s_addc_u32 s25, s25, s27
	s_lshl_b64 s[14:15], s[14:15], 12
	s_add_u32 s14, s7, s14
	s_addc_u32 s15, s25, s15
	v_lshl_add_u64 v[12:13], s[14:15], 0, v[8:9]
	v_cmp_eq_u64_e32 vcc, v[10:11], v[168:169]
	v_cmp_eq_u64_e64 s[98:99], v[12:13], v[170:171]
	s_nop 1
	s_and_b64 vcc, vcc, s[98:99]
	s_cmp_eq_u64 vcc, exec
	s_mov_b64 s[98:99], 0x2000
	v_lshl_add_u64 v[168:169], v[10:11], 0, s[98:99]
	v_lshl_add_u64 v[170:171], v[12:13], 0, s[98:99]
	s_cbranch_scc0 .Lrp0_miss
	s_waitcnt vmcnt(8)
	v_mov_b64_e32 v[40:41], v[136:137]
	v_mov_b64_e32 v[42:43], v[138:139]
	v_mov_b64_e32 v[44:45], v[140:141]
	v_mov_b64_e32 v[46:47], v[142:143]
	v_mov_b64_e32 v[32:33], v[144:145]
	v_mov_b64_e32 v[34:35], v[146:147]
	v_mov_b64_e32 v[36:37], v[148:149]
	v_mov_b64_e32 v[38:39], v[150:151]
	v_mov_b64_e32 v[16:17], v[152:153]
	v_mov_b64_e32 v[18:19], v[154:155]
	v_mov_b64_e32 v[20:21], v[156:157]
	v_mov_b64_e32 v[22:23], v[158:159]
	v_mov_b64_e32 v[8:9], v[160:161]
	v_mov_b64_e32 v[10:11], v[162:163]
	v_mov_b64_e32 v[12:13], v[164:165]
	v_mov_b64_e32 v[14:15], v[166:167]
	s_branch .Lrp0_join
.Lrp0_miss:
	global_load_dwordx4 v[40:43], v[10:11], off offset:16
	global_load_dwordx4 v[44:47], v[10:11], off
	global_load_dwordx4 v[32:35], v[10:11], off offset:2064
	global_load_dwordx4 v[36:39], v[10:11], off offset:2048
	global_load_dwordx4 v[16:19], v[12:13], off offset:16
	global_load_dwordx4 v[20:23], v[12:13], off
	s_nop 0
	global_load_dwordx4 v[8:11], v[12:13], off offset:2064
	s_nop 0
	global_load_dwordx4 v[12:15], v[12:13], off offset:2048
	s_waitcnt vmcnt(0)
.Lrp0_join:
	s_cmp_eq_u32 s13, s4
	s_cbranch_scc1 .LBB0_151
	s_mul_i32 s7, s13, 0x6000
	s_mul_hi_i32 s4, s13, 0x6000
	s_add_u32 s14, s60, s7
	global_load_dwordx4 v[24:27], v[48:49], off offset:16
	global_load_dwordx4 v[28:31], v[48:49], off
	s_addc_u32 s15, s63, s4
	v_lshl_add_u64 v[84:85], v[60:61], 2, s[14:15]
	v_add_co_u32_e32 v0, vcc, 0x1000, v84
	v_lshl_add_u64 v[58:59], v[84:85], 0, s[84:85]
	s_nop 0
	v_addc_co_u32_e32 v1, vcc, 0, v85, vcc
	global_load_dwordx4 v[54:57], v[0:1], off
	global_load_dwordx4 v[62:65], v[58:59], off offset:16
	global_load_dwordx4 v[4:7], v[84:85], off offset:16
	s_nop 0
	global_load_dwordx4 v[0:3], v[84:85], off
	global_load_dwordx4 v[72:75], v[48:49], off offset:2048
	global_load_dwordx4 v[66:69], v[48:49], off offset:2064
	global_load_dwordx4 v[76:79], v[58:59], off offset:2064
	global_load_dwordx4 v[80:83], v[58:59], off offset:2048
	s_mov_b32 s4, s13
	s_waitcnt vmcnt(0)
	v_pk_add_f32 v[56:57], v[56:57], 1.0 op_sel_hi:[1,0]
	v_pk_add_f32 v[54:55], v[54:55], 1.0 op_sel_hi:[1,0]
	s_waitcnt vmcnt(6)
	v_pk_add_f32 v[58:59], v[64:65], 1.0 op_sel_hi:[1,0]
	v_pk_add_f32 v[62:63], v[62:63], 1.0 op_sel_hi:[1,0]
	v_pk_mul_f32 v[56:57], v[30:31], v[56:57]
	v_pk_mul_f32 v[58:59], v[26:27], v[58:59]
	v_pk_mul_f32 v[54:55], v[28:29], v[54:55]
	v_pk_mul_f32 v[62:63], v[24:25], v[62:63]
	global_load_dwordx4 v[24:27], v[84:85], off offset:2064
	global_load_dwordx4 v[28:31], v[84:85], off offset:2048
	s_waitcnt vmcnt(2)
	v_pk_add_f32 v[64:65], v[82:83], 1.0 op_sel_hi:[1,0]
	v_pk_add_f32 v[70:71], v[78:79], 1.0 op_sel_hi:[1,0]
	v_pk_add_f32 v[78:79], v[80:81], 1.0 op_sel_hi:[1,0]
	v_pk_add_f32 v[76:77], v[76:77], 1.0 op_sel_hi:[1,0]
	v_pk_mul_f32 v[68:69], v[68:69], v[70:71]
	v_pk_mul_f32 v[64:65], v[74:75], v[64:65]
	v_pk_mul_f32 v[70:71], v[66:67], v[76:77]
	v_pk_mul_f32 v[66:67], v[72:73], v[78:79]
.LBB0_151:
	s_waitcnt vmcnt(0)
	s_cmp_ge_i32 s2, s12
	s_cbranch_scc1 .Lrp0_nopf
	s_cmp_eq_u32 s13, 16
	s_cbranch_scc1 .Lrp0_nopf
	s_cmp_lg_u64 s[38:39], 0
	s_cbranch_scc1 .Lrp0_nopf
	global_load_dwordx4 v[136:139], v[168:169], off offset:16
	global_load_dwordx4 v[140:143], v[168:169], off
	global_load_dwordx4 v[144:147], v[168:169], off offset:2064
	global_load_dwordx4 v[148:151], v[168:169], off offset:2048
	global_load_dwordx4 v[152:155], v[170:171], off offset:16
	global_load_dwordx4 v[156:159], v[170:171], off
	global_load_dwordx4 v[160:163], v[170:171], off offset:2064
	global_load_dwordx4 v[164:167], v[170:171], off offset:2048
	s_branch .Lrp0_pfdone
.Lrp0_nopf:
	v_mov_b32_e32 v168, 0
	v_mov_b32_e32 v169, 0
.Lrp0_pfdone:
	v_mul_f32_e32 v72, v45, v45
	v_mul_f32_e32 v73, v47, v47
	v_fmac_f32_e32 v72, v44, v44
	v_fmac_f32_e32 v73, v46, v46
	v_add_f32_e32 v72, v72, v73
	v_mul_f32_e32 v73, v41, v41
	v_mul_f32_e32 v74, v43, v43
	v_fmac_f32_e32 v73, v40, v40
	v_fmac_f32_e32 v74, v42, v42
	v_add_f32_e32 v73, v73, v74
	v_add_f32_e32 v72, v72, v73
	v_mul_f32_e32 v73, v37, v37
	v_mul_f32_e32 v74, v39, v39
	v_fmac_f32_e32 v73, v36, v36
	v_fmac_f32_e32 v74, v38, v38
	v_add_f32_e32 v73, v73, v74
	v_add_f32_e32 v72, v72, v73
	v_mul_f32_e32 v73, v33, v33
	v_mul_f32_e32 v74, v35, v35
	v_fmac_f32_e32 v73, v32, v32
	v_fmac_f32_e32 v74, v34, v34
	v_add_f32_e32 v73, v73, v74
	v_add_f32_e32 v72, v72, v73
	s_nop 1
	v_mov_b32_dpp v73, v72 quad_perm:[1,0,3,2] row_mask:0xf bank_mask:0xf
	s_and_b64 s[14:15], s[38:39], exec
	s_mov_b32 s7, s4
	s_cselect_b32 s4, 16, s6
	s_mov_b32 s6, 0x17dd9000
	s_waitcnt lgkmcnt(0)
	v_add_f32_e32 v72, v72, v73
	s_nop 1
	v_mov_b32_dpp v73, v72 quad_perm:[2,3,0,1] row_mask:0xf bank_mask:0xf
	s_cmp_eq_u32 s4, s7
	s_waitcnt lgkmcnt(0)
	v_add_f32_e32 v72, v72, v73
	s_nop 1
	v_mov_b32_dpp v73, v72 row_half_mirror row_mask:0xf bank_mask:0xf
	s_waitcnt lgkmcnt(0)
	v_add_f32_e32 v72, v72, v73
	s_nop 1
	v_mov_b32_dpp v73, v72 row_mirror row_mask:0xf bank_mask:0xf
	s_waitcnt lgkmcnt(0)
	v_add_f32_e32 v72, v72, v73
	ds_swizzle_b32 v73, v72 offset:swizzle(SWAP,16)
	s_waitcnt lgkmcnt(0)
	v_add_f32_e32 v72, v72, v73
	v_mov_b32_e32 v73, v72
	s_nop 1
	v_permlane32_swap_b32_e32 v72, v73
	v_add_f32_e32 v72, v72, v73
	v_fmamk_f32 v72, v72, 0x3a800000, v196
	v_cmp_gt_f32_e32 vcc, s35, v72
	v_mul_f32_e32 v73, 0x4b800000, v72
	s_nop 0
	v_cndmask_b32_e32 v72, v72, v73, vcc
	v_rsq_f32_e32 v72, v72
	s_nop 0
	v_mul_f32_e32 v73, 0x45800000, v72
	v_cndmask_b32_e32 v72, v72, v73, vcc
	v_pk_mul_f32 v[42:43], v[42:43], v[72:73] op_sel_hi:[1,0]
	v_pk_mul_f32 v[44:45], v[44:45], v[72:73] op_sel_hi:[1,0]
	v_pk_mul_f32 v[46:47], v[46:47], v[72:73] op_sel_hi:[1,0]
	v_pk_mul_f32 v[40:41], v[40:41], v[72:73] op_sel_hi:[1,0]
	v_pk_fma_f32 v[78:79], v[58:59], v[42:43], v[6:7]
	v_lshl_add_u64 v[42:43], s[94:95], 0, v[52:53]
	v_pk_fma_f32 v[74:75], v[56:57], v[46:47], v[2:3]
	v_pk_fma_f32 v[76:77], v[54:55], v[44:45], v[0:1]
	v_pk_fma_f32 v[40:41], v[62:63], v[40:41], v[4:5]
	v_add_co_u32_e32 v42, vcc, s6, v42
	v_cvt_pk_bf16_f32 v44, v76, v77
	v_cvt_pk_bf16_f32 v45, v74, v75
	v_cvt_pk_bf16_f32 v46, v40, v41
	v_cvt_pk_bf16_f32 v47, v78, v79
	v_addc_co_u32_e32 v43, vcc, 0, v43, vcc
	global_store_dwordx4 v[42:43], v[44:47], off
	s_mov_b32 s6, 0x711d9000
	v_pk_mul_f32 v[36:37], v[36:37], v[72:73] op_sel_hi:[1,0]
	v_mov_b32_e32 v44, v113
	v_mov_b32_e32 v45, v113
	v_cvt_pk_fp8_f32 v44, v76, v77
	v_cvt_pk_fp8_f32 v45, v40, v41
	v_lshl_add_u64 v[40:41], s[94:95], 0, v[50:51]
	v_add_co_u32_e32 v40, vcc, s6, v40
	v_cvt_pk_fp8_f32 v44, v74, v75 op_sel:[0,0,1]
	v_cvt_pk_fp8_f32 v45, v78, v79 op_sel:[0,0,1]
	v_addc_co_u32_e32 v41, vcc, 0, v41, vcc
	v_pk_mul_f32 v[38:39], v[38:39], v[72:73] op_sel_hi:[1,0]
	v_pk_mul_f32 v[32:33], v[32:33], v[72:73] op_sel_hi:[1,0]
	v_pk_mul_f32 v[34:35], v[34:35], v[72:73] op_sel_hi:[1,0]
	global_store_dwordx2 v[40:41], v[44:45], off
	s_waitcnt vmcnt(2)
	v_pk_fma_f32 v[38:39], v[64:65], v[38:39], v[30:31]
	v_pk_fma_f32 v[36:37], v[66:67], v[36:37], v[28:29]
	v_pk_fma_f32 v[44:45], v[68:69], v[34:35], v[26:27]
	v_pk_fma_f32 v[46:47], v[70:71], v[32:33], v[24:25]
	v_cvt_pk_bf16_f32 v32, v36, v37
	v_cvt_pk_bf16_f32 v33, v38, v39
	v_cvt_pk_bf16_f32 v34, v46, v47
	v_cvt_pk_bf16_f32 v35, v44, v45
	global_store_dwordx4 v[42:43], v[32:35], off offset:1024
	s_nop 1
	v_mov_b32_e32 v32, v113
	v_mov_b32_e32 v33, v113
	v_cvt_pk_fp8_f32 v32, v36, v37
	v_cvt_pk_fp8_f32 v33, v46, v47
	v_cvt_pk_fp8_f32 v32, v38, v39 op_sel:[0,0,1]
	v_cvt_pk_fp8_f32 v33, v44, v45 op_sel:[0,0,1]
	global_store_dwordx2 v[40:41], v[32:33], off offset:512
	s_cbranch_scc1 .LBB0_148
	s_mul_i32 s6, s4, 0x6000
	s_mul_hi_i32 s7, s4, 0x6000
	s_add_u32 s6, s60, s6
	s_addc_u32 s7, s63, s7
	v_lshl_add_u64 v[44:45], v[60:61], 2, s[6:7]
	v_add_co_u32_e32 v24, vcc, 0x1000, v44
	global_load_dwordx4 v[0:3], v[48:49], off offset:16
	global_load_dwordx4 v[4:7], v[48:49], off
	v_addc_co_u32_e32 v25, vcc, 0, v45, vcc
	v_lshl_add_u64 v[36:37], v[44:45], 0, s[84:85]
	global_load_dwordx4 v[24:27], v[24:25], off
	s_nop 0
	global_load_dwordx4 v[28:31], v[36:37], off offset:16
	s_waitcnt vmcnt(1)
	v_pk_add_f32 v[26:27], v[26:27], 1.0 op_sel_hi:[1,0]
	v_pk_add_f32 v[24:25], v[24:25], 1.0 op_sel_hi:[1,0]
	v_pk_mul_f32 v[56:57], v[6:7], v[26:27]
	v_pk_mul_f32 v[54:55], v[4:5], v[24:25]
	s_waitcnt vmcnt(0)
	v_pk_add_f32 v[4:5], v[30:31], 1.0 op_sel_hi:[1,0]
	v_pk_add_f32 v[6:7], v[28:29], 1.0 op_sel_hi:[1,0]
	v_pk_mul_f32 v[58:59], v[2:3], v[4:5]
	v_pk_mul_f32 v[62:63], v[0:1], v[6:7]
	global_load_dwordx4 v[4:7], v[44:45], off offset:16
	global_load_dwordx4 v[0:3], v[44:45], off
	global_load_dwordx4 v[24:27], v[48:49], off offset:2064
	global_load_dwordx4 v[28:31], v[48:49], off offset:2048
	global_load_dwordx4 v[32:35], v[36:37], off offset:2064
	s_nop 0
	global_load_dwordx4 v[36:39], v[36:37], off offset:2048
	s_waitcnt vmcnt(0)
	v_pk_add_f32 v[38:39], v[38:39], 1.0 op_sel_hi:[1,0]
	v_pk_add_f32 v[36:37], v[36:37], 1.0 op_sel_hi:[1,0]
	v_pk_mul_f32 v[64:65], v[30:31], v[38:39]
	v_pk_mul_f32 v[66:67], v[28:29], v[36:37]
	v_pk_add_f32 v[28:29], v[34:35], 1.0 op_sel_hi:[1,0]
	v_pk_add_f32 v[30:31], v[32:33], 1.0 op_sel_hi:[1,0]
	v_pk_mul_f32 v[68:69], v[26:27], v[28:29]
	v_pk_mul_f32 v[70:71], v[24:25], v[30:31]
	global_load_dwordx4 v[24:27], v[44:45], off offset:2064
	global_load_dwordx4 v[28:31], v[44:45], off offset:2048
	s_branch .LBB0_148
